# router phase: the 24 loop-invariant per-chunk vector loads hoisted out of the token loops into persistent registers (was a load+wait ladder per token)
# speedup vs baseline: 1.0078x; 1.0078x over previous
.LBB0_1405:
	s_or_b64 exec, exec, s[4:5]
	s_cmpk_gt_i32 s2, 0x3ff
	s_waitcnt vmcnt(0) lgkmcnt(0)
	s_barrier
	s_cbranch_scc1 .LBB0_1494
	s_add_u32 s6, s50, 0x106000
	s_addc_u32 s7, s51, 0
	s_add_u32 s16, s50, 0x108000
	s_addc_u32 s17, s51, 0
	s_add_u32 s12, s50, 0x110000
	s_addc_u32 s13, s51, 0
	v_mov_b32_e32 v3, 0
	s_add_u32 s14, s50, 0x150000
	v_readlane_b32 s18, v237, 37
	v_lshlrev_b32_e32 v4, 3, v194
	v_mov_b32_e32 v5, v3
	v_lshrrev_b32_e32 v7, 2, v0
	s_addc_u32 s15, s51, 0
	v_lshl_add_u64 v[12:13], s[42:43], 0, v[4:5]
	v_and_b32_e32 v5, 15, v0
	s_lshl_b32 s4, s18, 10
	v_and_b32_e32 v8, 12, v7
	v_lshlrev_b32_e32 v6, 13, v5
	s_add_i32 s4, s4, 0
	v_lshlrev_b32_e32 v7, 2, v8
	v_lshlrev_b32_e32 v9, 2, v5
	v_and_b32_e32 v71, 31, v0
	v_and_b32_e32 v5, 0x1e0, v0
	v_lshlrev_b32_e32 v2, 4, v194
	v_readlane_b32 s52, v237, 5
	v_add3_u32 v69, s4, v6, v7
	s_add_i32 s4, 0, 0x20000
	v_lshlrev_b32_e32 v6, 2, v71
	v_mov_b32_e32 v7, v3
	v_lshlrev_b32_e32 v5, 2, v5
	v_readlane_b32 s53, v237, 6
	v_readlane_b32 s54, v237, 7
	v_readlane_b32 s55, v237, 8
	v_readlane_b32 s56, v237, 9
	v_readlane_b32 s57, v237, 10
	v_readlane_b32 s58, v237, 11
	v_readlane_b32 s59, v237, 12
	v_readlane_b32 s60, v237, 13
	v_readlane_b32 s61, v237, 14
	v_readlane_b32 s62, v237, 15
	v_readlane_b32 s63, v237, 16
	v_readlane_b32 s64, v237, 17
	v_readlane_b32 s65, v237, 18
	v_readlane_b32 s66, v237, 19
	v_readlane_b32 s67, v237, 20
	v_lshl_add_u64 v[14:15], s[36:37], 0, v[6:7]
	v_add3_u32 v72, s4, v5, v6
	v_or_b32_e32 v6, 0x400, v2
	v_lshl_add_u64 v[10:11], s[52:53], 0, v[2:3]
	v_readlane_b32 s52, v237, 21
	v_lshl_add_u64 v[22:23], s[16:17], 0, v[6:7]
	v_lshl_add_u64 v[24:25], s[6:7], 0, v[6:7]
	v_or_b32_e32 v6, 0x800, v2
	v_readlane_b32 s64, v237, 33
	v_readlane_b32 s65, v237, 34
	v_lshl_add_u64 v[26:27], s[16:17], 0, v[6:7]
	v_lshl_add_u64 v[28:29], s[6:7], 0, v[6:7]
	v_or_b32_e32 v6, 0xc00, v2
	v_readlane_b32 s66, v237, 35
	v_readlane_b32 s67, v237, 36
	s_mov_b64 s[24:25], s[64:65]
	v_lshl_add_u64 v[30:31], s[16:17], 0, v[6:7]
	v_lshl_add_u64 v[32:33], s[6:7], 0, v[6:7]
	v_or_b32_e32 v6, 0x1000, v2
	v_lshl_add_u64 v[34:35], s[24:25], 0, v[6:7]
	v_lshl_add_u64 v[36:37], s[16:17], 0, v[6:7]
	v_lshl_add_u64 v[38:39], s[6:7], 0, v[6:7]
	v_or_b32_e32 v6, 0x1400, v2
	v_lshl_add_u64 v[40:41], s[24:25], 0, v[6:7]
	v_lshl_add_u64 v[42:43], s[16:17], 0, v[6:7]
	v_lshl_add_u64 v[44:45], s[6:7], 0, v[6:7]
	v_or_b32_e32 v6, 0x1800, v2
	v_lshl_add_u64 v[16:17], s[24:25], 0, v[2:3]
	v_lshl_add_u64 v[18:19], s[16:17], 0, v[2:3]
	v_lshl_add_u64 v[20:21], s[6:7], 0, v[2:3]
	v_lshl_add_u64 v[46:47], s[24:25], 0, v[6:7]
	v_lshl_add_u64 v[48:49], s[16:17], 0, v[6:7]
	v_lshl_add_u64 v[50:51], s[6:7], 0, v[6:7]
	v_or_b32_e32 v6, 0x1c00, v2
	v_add_u32_e32 v73, 0, v2
	v_lshl_or_b32 v2, s18, 8, v8
	v_mov_b32_e32 v5, v3
	v_lshlrev_b64 v[2:3], 7, v[2:3]
	s_mov_b64 s[26:27], s[66:67]
	v_lshl_add_u64 v[52:53], s[24:25], 0, v[6:7]
	v_lshl_add_u64 v[54:55], s[16:17], 0, v[6:7]
	v_lshl_add_u64 v[56:57], s[6:7], 0, v[6:7]
	v_lshlrev_b32_e32 v6, 7, v8
	v_or_b32_e32 v2, v2, v9
	v_lshlrev_b32_e32 v4, 2, v194
	v_add_u32_e32 v62, s4, v9
	v_lshl_or_b32 v6, s18, 11, v6
	v_lshl_add_u64 v[60:61], s[26:27], 0, v[2:3]
	v_mbcnt_lo_u32_b32 v2, -1, 0
	s_lshl_b32 s3, s18, 1
	v_lshrrev_b32_e32 v70, 5, v0
	v_cmp_eq_u32_e64 s[4:5], 0, v71
	s_movk_i32 s20, 0x1000
	v_lshl_add_u64 v[58:59], s[8:9], 0, v[4:5]
	v_mov_b32_e32 v74, 0x3727c5ac
	s_mov_b32 s21, 0x800000
	v_add_u32_e32 v75, v62, v6
	v_mbcnt_hi_u32_b32 v76, -1, v2
	s_add_i32 s22, 0, 0x25e80
	v_mov_b32_e32 v77, 1
	v_mov_b32_e32 v78, 0x3a000000
	v_mov_b32_e32 v79, 0xff800000
	s_mov_b32 s23, s2
	v_readlane_b32 s53, v237, 22
	v_readlane_b32 s54, v237, 23
	v_readlane_b32 s55, v237, 24
	v_readlane_b32 s56, v237, 25
	v_readlane_b32 s57, v237, 26
	v_readlane_b32 s58, v237, 27
	v_readlane_b32 s59, v237, 28
	v_readlane_b32 s60, v237, 29
	v_readlane_b32 s61, v237, 30
	v_readlane_b32 s62, v237, 31
	v_readlane_b32 s63, v237, 32
	global_load_dwordx4 v[148:151], v[16:17], off
	global_load_dwordx4 v[152:155], v[18:19], off
	global_load_dwordx4 v[156:159], v[20:21], off
	global_load_dwordx4 v[160:163], v[16:17], off offset:1024
	global_load_dwordx4 v[164:167], v[22:23], off
	global_load_dwordx4 v[168:171], v[24:25], off
	global_load_dwordx4 v[172:175], v[16:17], off offset:2048
	global_load_dwordx4 v[176:179], v[26:27], off
	global_load_dwordx4 v[180:183], v[28:29], off
	global_load_dwordx4 v[184:187], v[16:17], off offset:3072
	global_load_dwordx4 v[188:191], v[30:31], off
	global_load_dwordx4 v[196:199], v[32:33], off
	global_load_dwordx4 v[200:203], v[34:35], off
	global_load_dwordx4 v[204:207], v[36:37], off
	global_load_dwordx4 v[208:211], v[38:39], off
	global_load_dwordx4 v[212:215], v[40:41], off
	global_load_dwordx4 v[216:219], v[42:43], off
	global_load_dwordx4 v[220:223], v[44:45], off
	global_load_dwordx4 v[224:227], v[46:47], off
	global_load_dwordx4 v[228:231], v[48:49], off
	global_load_dwordx4 v[232:235], v[50:51], off
	global_load_dwordx4 v[238:241], v[52:53], off
	global_load_dwordx4 v[242:245], v[54:55], off
	global_load_dwordx4 v[246:249], v[56:57], off
	s_waitcnt vmcnt(0)
	s_branch .LBB0_1408

.LBB0_1409:
	s_or_b32 s16, s17, s3
	s_add_i32 s18, s16, s24
	s_ashr_i32 s19, s18, 31
	s_lshl_b64 s[26:27], s[18:19], 11
	s_lshl_b64 s[34:35], s[18:19], 13
	s_lshl_b64 s[18:19], s[18:19], 12
	v_lshl_add_u64 v[8:9], v[10:11], 0, s[34:35]
	v_lshl_add_u64 v[104:105], v[12:13], 0, s[18:19]
	global_load_dwordx2 v[66:67], v[104:105], off
	global_load_dwordx2 v[106:107], v[104:105], off offset:512
	global_load_dwordx2 v[108:109], v[104:105], off offset:1024
	global_load_dwordx2 v[110:111], v[104:105], off offset:1536
	global_load_dwordx2 v[112:113], v[104:105], off offset:2048
	global_load_dwordx2 v[114:115], v[104:105], off offset:2560
	global_load_dwordx2 v[116:117], v[104:105], off offset:3072
	global_load_dwordx2 v[118:119], v[104:105], off offset:3584
	global_load_dwordx4 v[4:7], v[8:9], off
	global_load_dwordx4 v[62:65], v[8:9], off offset:1024
	global_load_dwordx4 v[80:83], v[8:9], off offset:2048
	global_load_dwordx4 v[84:87], v[8:9], off offset:3072
	v_add_co_u32_e32 v8, vcc, s20, v8
	v_mov_b32_e32 v138, 0
	s_nop 0
	v_addc_co_u32_e32 v9, vcc, 0, v9, vcc
	global_load_dwordx4 v[88:91], v[8:9], off
	global_load_dwordx4 v[92:95], v[8:9], off offset:1024
	global_load_dwordx4 v[96:99], v[8:9], off offset:2048
	global_load_dwordx4 v[100:103], v[8:9], off offset:3072
	v_mov_b32_e32 v139, 0
	v_mov_b32_e32 v140, 0
	v_lshl_add_u64 v[2:3], v[58:59], 0, s[26:27]
	s_waitcnt vmcnt(15)
	v_lshlrev_b32_e32 v8, 16, v66
	v_and_b32_e32 v9, 0xffff0000, v66
	s_waitcnt vmcnt(13)
	v_lshlrev_b32_e32 v122, 16, v108
	v_and_b32_e32 v123, 0xffff0000, v108
	v_lshlrev_b32_e32 v108, 16, v109
	v_and_b32_e32 v109, 0xffff0000, v109
	v_lshlrev_b32_e32 v66, 16, v67
	v_and_b32_e32 v67, 0xffff0000, v67
	s_waitcnt vmcnt(10)
	v_lshlrev_b32_e32 v128, 16, v114
	v_and_b32_e32 v129, 0xffff0000, v114
	s_waitcnt vmcnt(5)
	v_pk_add_f32 v[108:109], v[82:83], v[108:109]
	v_pk_add_f32 v[122:123], v[80:81], v[122:123]
	v_lshlrev_b32_e32 v120, 16, v106
	v_and_b32_e32 v121, 0xffff0000, v106
	v_lshlrev_b32_e32 v106, 16, v107
	v_and_b32_e32 v107, 0xffff0000, v107
	v_lshlrev_b32_e32 v124, 16, v110
	v_and_b32_e32 v125, 0xffff0000, v110
	v_pk_add_f32 v[134:135], v[6:7], v[66:67]
	s_waitcnt vmcnt(2)
	v_pk_add_f32 v[66:67], v[92:93], v[128:129]
	v_pk_mul_f32 v[80:81], v[108:109], v[108:109]
	v_pk_mul_f32 v[92:93], v[122:123], v[122:123]
	v_pk_add_f32 v[136:137], v[4:5], v[8:9]
	v_pk_add_f32 v[106:107], v[64:65], v[106:107]
	v_pk_add_f32 v[120:121], v[62:63], v[120:121]
	v_pk_add_f32 v[124:125], v[84:85], v[124:125]
	v_cvt_pk_bf16_f32 v84, v136, v137
	v_cvt_pk_bf16_f32 v85, v134, v135
	v_pk_mov_b32 v[128:129], v[92:93], v[80:81] op_sel:[1,0]
	v_mov_b32_e32 v93, v81
	global_store_dwordx2 v[104:105], v[84:85], off
	v_cvt_pk_bf16_f32 v80, v120, v121
	v_cvt_pk_bf16_f32 v81, v106, v107
	v_lshlrev_b32_e32 v110, 16, v111
	v_and_b32_e32 v111, 0xffff0000, v111
	global_store_dwordx2 v[104:105], v[80:81], off offset:512
	v_cvt_pk_bf16_f32 v80, v122, v123
	v_cvt_pk_bf16_f32 v81, v108, v109
	v_lshlrev_b32_e32 v126, 16, v112
	v_and_b32_e32 v127, 0xffff0000, v112
	v_lshlrev_b32_e32 v112, 16, v113
	v_and_b32_e32 v113, 0xffff0000, v113
	v_pk_add_f32 v[110:111], v[86:87], v[110:111]
	global_store_dwordx2 v[104:105], v[80:81], off offset:1024
	v_cvt_pk_bf16_f32 v80, v124, v125
	v_cvt_pk_bf16_f32 v81, v110, v111
	v_lshlrev_b32_e32 v114, 16, v115
	v_and_b32_e32 v115, 0xffff0000, v115
	v_pk_add_f32 v[112:113], v[90:91], v[112:113]
	v_pk_add_f32 v[126:127], v[88:89], v[126:127]
	global_store_dwordx2 v[104:105], v[80:81], off offset:1536
	v_cvt_pk_bf16_f32 v80, v126, v127
	v_cvt_pk_bf16_f32 v81, v112, v113
	v_lshlrev_b32_e32 v130, 16, v116
	v_and_b32_e32 v131, 0xffff0000, v116
	v_lshlrev_b32_e32 v116, 16, v117
	v_and_b32_e32 v117, 0xffff0000, v117
	v_pk_add_f32 v[64:65], v[94:95], v[114:115]
	global_store_dwordx2 v[104:105], v[80:81], off offset:2048
	v_cvt_pk_bf16_f32 v80, v66, v67
	v_cvt_pk_bf16_f32 v81, v64, v65
	v_lshlrev_b32_e32 v132, 16, v118
	v_and_b32_e32 v133, 0xffff0000, v118
	v_lshlrev_b32_e32 v118, 16, v119
	v_and_b32_e32 v119, 0xffff0000, v119
	s_waitcnt vmcnt(6)
	v_pk_add_f32 v[8:9], v[98:99], v[116:117]
	v_pk_add_f32 v[62:63], v[96:97], v[130:131]
	global_store_dwordx2 v[104:105], v[80:81], off offset:2560
	v_cvt_pk_bf16_f32 v80, v62, v63
	v_cvt_pk_bf16_f32 v81, v8, v9
	s_waitcnt vmcnt(6)
	v_pk_add_f32 v[4:5], v[102:103], v[118:119]
	v_pk_add_f32 v[6:7], v[100:101], v[132:133]
	v_pk_mul_f32 v[94:95], v[66:67], v[66:67]
	v_pk_mul_f32 v[82:83], v[64:65], v[64:65]
	global_store_dwordx2 v[104:105], v[80:81], off offset:3072
	v_cvt_pk_bf16_f32 v80, v6, v7
	v_cvt_pk_bf16_f32 v81, v4, v5
	global_store_dwordx2 v[104:105], v[80:81], off offset:3584
	v_pk_mov_b32 v[130:131], v[94:95], v[82:83] op_sel:[1,0]
	v_mov_b32_e32 v95, v83
	v_mov_b32_e32 v80, v148
	v_mov_b32_e32 v81, v149
	v_mov_b32_e32 v82, v150
	v_mov_b32_e32 v83, v151
	v_mov_b32_e32 v84, v152
	v_mov_b32_e32 v85, v153
	v_mov_b32_e32 v86, v154
	v_mov_b32_e32 v87, v155
	v_mov_b32_e32 v88, v156
	v_mov_b32_e32 v89, v157
	v_mov_b32_e32 v90, v158
	v_mov_b32_e32 v91, v159
	v_mov_b32_e32 v96, v137
	v_mov_b32_e32 v97, v121
	v_mov_b32_e32 v100, v135
	v_mov_b32_e32 v101, v107
	v_mov_b32_e32 v98, v134
	v_mov_b32_e32 v99, v106
	v_mov_b32_e32 v102, v136
	v_mov_b32_e32 v103, v120
	v_pk_mul_f32 v[96:97], v[96:97], v[96:97]
	v_pk_mul_f32 v[100:101], v[100:101], v[100:101]
	v_pk_fma_f32 v[96:97], v[102:103], v[102:103], v[96:97]
	v_pk_fma_f32 v[98:99], v[98:99], v[98:99], v[100:101]
	v_mul_f32_e32 v68, v125, v125
	v_mul_f32_e32 v114, v111, v111
	v_pk_add_f32 v[92:93], v[128:129], v[92:93]
	v_pk_add_f32 v[96:97], v[96:97], v[98:99]
	v_mul_f32_e32 v132, v126, v126
	v_mul_f32_e32 v133, v127, v127
	v_mul_f32_e32 v141, v112, v112
	v_mul_f32_e32 v142, v113, v113
	v_pk_fma_f32 v[104:105], v[124:125], v[124:125], v[68:69] op_sel_hi:[1,1,0]
	v_pk_fma_f32 v[114:115], v[110:111], v[110:111], v[114:115] op_sel_hi:[1,1,0]
	v_pk_add_f32 v[92:93], v[92:93], v[92:93] op_sel:[0,1] op_sel_hi:[1,0]
	v_pk_add_f32 v[96:97], v[96:97], v[96:97] op_sel:[0,1] op_sel_hi:[1,0]
	v_mov_b32_e32 v105, v141
	v_mov_b32_e32 v115, v142
	v_mov_b32_e32 v93, v133
	v_mov_b32_e32 v97, v132
	v_pk_add_f32 v[98:99], v[104:105], v[114:115]
	v_pk_add_f32 v[92:93], v[96:97], v[92:93]
	v_mul_f32_e32 v116, v63, v63
	v_mul_f32_e32 v118, v9, v9
	v_pk_add_f32 v[94:95], v[130:131], v[94:95]
	v_pk_add_f32 v[92:93], v[92:93], v[98:99]
	v_mul_f32_e32 v143, v6, v6
	v_mul_f32_e32 v144, v7, v7
	v_mul_f32_e32 v145, v4, v4
	v_mul_f32_e32 v146, v5, v5
	v_pk_fma_f32 v[116:117], v[62:63], v[62:63], v[116:117] op_sel_hi:[1,1,0]
	v_pk_fma_f32 v[118:119], v[8:9], v[8:9], v[118:119] op_sel_hi:[1,1,0]
	v_pk_add_f32 v[94:95], v[94:95], v[94:95] op_sel:[0,1] op_sel_hi:[1,0]
	v_pk_add_f32 v[92:93], v[92:93], v[92:93] op_sel:[0,1] op_sel_hi:[1,0]
	v_mov_b32_e32 v117, v145
	v_mov_b32_e32 v119, v146
	v_mov_b32_e32 v95, v144
	v_mov_b32_e32 v93, v143
	v_pk_add_f32 v[100:101], v[116:117], v[118:119]
	v_pk_add_f32 v[92:93], v[92:93], v[94:95]
	v_mov_b32_e32 v104, 0
	v_pk_add_f32 v[92:93], v[92:93], v[100:101]
	v_mov_b32_e32 v100, 0
	v_add_f32_e32 v68, v92, v93
	v_mov_b32_e32 v114, 0
	v_pk_add_f32 v[84:85], v[84:85], 1.0 op_sel_hi:[1,0]
	v_add_f32_dpp v68, v68, v68 row_shr:1 row_mask:0xf bank_mask:0xf bound_ctrl:1
	v_pk_add_f32 v[86:87], v[86:87], 1.0 op_sel_hi:[1,0]
	s_nop 0
	v_add_f32_dpp v68, v68, v68 row_shr:2 row_mask:0xf bank_mask:0xf bound_ctrl:1
	s_nop 1
	v_add_f32_dpp v68, v68, v68 row_shr:4 row_mask:0xf bank_mask:0xf bound_ctrl:1
	s_nop 1
	v_add_f32_dpp v68, v68, v68 row_shr:8 row_mask:0xf bank_mask:0xf bound_ctrl:1
	s_nop 1
	v_mov_b32_dpp v138, v68 row_bcast:15 row_mask:0xa bank_mask:0xf
	v_add_f32_e32 v68, v68, v138
	s_nop 1
	v_mov_b32_dpp v139, v68 row_bcast:31 row_mask:0xc bank_mask:0xf
	v_add_f32_e32 v68, v68, v139
	s_nop 0
	v_readlane_b32 s17, v68, 63
	s_nop 1
	v_fma_f32 v68, s17, v78, v74
	v_mul_f32_e32 v92, 0x4b800000, v68
	v_cmp_gt_f32_e32 vcc, s21, v68
	s_mov_b32 s17, 1
	s_nop 0
	v_cndmask_b32_e32 v68, v68, v92, vcc
	v_rsq_f32_e32 v68, v68
	s_nop 0
	v_mul_f32_e32 v92, 0x45800000, v68
	v_cndmask_b32_e32 v68, v68, v92, vcc
	v_pk_mul_f32 v[92:93], v[68:69], v[136:137] op_sel_hi:[0,1]
	v_pk_mul_f32 v[80:81], v[80:81], v[92:93]
	v_pk_mul_f32 v[94:95], v[68:69], v[134:135] op_sel_hi:[0,1]
	v_pk_fma_f32 v[80:81], v[84:85], v[80:81], v[88:89]
	v_pk_mul_f32 v[82:83], v[82:83], v[94:95]
	v_cvt_pk_fp8_f32 v140, v80, v81
	v_pk_fma_f32 v[82:83], v[86:87], v[82:83], v[90:91]
	v_pk_mul_f32 v[96:97], v[68:69], v[120:121] op_sel_hi:[0,1]
	v_pk_mul_f32 v[98:99], v[68:69], v[106:107] op_sel_hi:[0,1]
	v_cvt_pk_fp8_f32 v140, v82, v83 op_sel:[0,0,1]
	v_pk_mul_f32 v[102:103], v[68:69], v[108:109] op_sel_hi:[0,1]
	v_mov_b32_e32 v108, 0
	v_pk_mul_f32 v[106:107], v[68:69], v[110:111] op_sel_hi:[0,1]
	global_store_dword v[2:3], v140, off
	v_mov_b32_e32 v84, v160
	v_mov_b32_e32 v85, v161
	v_mov_b32_e32 v86, v162
	v_mov_b32_e32 v87, v163
	v_mov_b32_e32 v88, v164
	v_mov_b32_e32 v89, v165
	v_mov_b32_e32 v90, v166
	v_mov_b32_e32 v91, v167
	v_mov_b32_e32 v92, v168
	v_mov_b32_e32 v93, v169
	v_mov_b32_e32 v94, v170
	v_mov_b32_e32 v95, v171
	v_pk_mul_f32 v[110:111], v[68:69], v[112:113] op_sel_hi:[0,1]
	v_pk_mul_f32 v[66:67], v[68:69], v[66:67] op_sel_hi:[0,1]
	v_pk_mul_f32 v[64:65], v[68:69], v[64:65] op_sel_hi:[0,1]
	v_mov_b32_e32 v112, 0
	v_pk_mul_f32 v[62:63], v[68:69], v[62:63] op_sel_hi:[0,1]
	v_pk_mul_f32 v[8:9], v[68:69], v[8:9] op_sel_hi:[0,1]
	v_pk_mul_f32 v[6:7], v[68:69], v[6:7] op_sel_hi:[0,1]
	v_pk_mul_f32 v[84:85], v[84:85], v[96:97]
	v_pk_add_f32 v[88:89], v[88:89], 1.0 op_sel_hi:[1,0]
	v_pk_mul_f32 v[86:87], v[86:87], v[98:99]
	v_pk_fma_f32 v[84:85], v[88:89], v[84:85], v[92:93]
	v_pk_add_f32 v[90:91], v[90:91], 1.0 op_sel_hi:[1,0]
	v_cvt_pk_fp8_f32 v100, v84, v85
	v_pk_fma_f32 v[86:87], v[90:91], v[86:87], v[94:95]
	s_nop 0
	v_cvt_pk_fp8_f32 v100, v86, v87 op_sel:[0,0,1]
	global_store_dword v[2:3], v100, off offset:256
	v_mov_b32_e32 v88, v172
	v_mov_b32_e32 v89, v173
	v_mov_b32_e32 v90, v174
	v_mov_b32_e32 v91, v175
	v_mov_b32_e32 v92, v176
	v_mov_b32_e32 v93, v177
	v_mov_b32_e32 v94, v178
	v_mov_b32_e32 v95, v179
	v_mov_b32_e32 v96, v180
	v_mov_b32_e32 v97, v181
	v_mov_b32_e32 v98, v182
	v_mov_b32_e32 v99, v183
	v_pk_mul_f32 v[100:101], v[68:69], v[122:123] op_sel_hi:[0,1]
	v_pk_mul_f32 v[88:89], v[88:89], v[100:101]
	v_pk_add_f32 v[92:93], v[92:93], 1.0 op_sel_hi:[1,0]
	v_pk_mul_f32 v[90:91], v[90:91], v[102:103]
	v_pk_fma_f32 v[88:89], v[92:93], v[88:89], v[96:97]
	v_pk_add_f32 v[94:95], v[94:95], 1.0 op_sel_hi:[1,0]
	v_cvt_pk_fp8_f32 v104, v88, v89
	v_pk_fma_f32 v[90:91], v[94:95], v[90:91], v[98:99]
	s_nop 0
	v_cvt_pk_fp8_f32 v104, v90, v91 op_sel:[0,0,1]
	global_store_dword v[2:3], v104, off offset:512
	v_mov_b32_e32 v92, v184
	v_mov_b32_e32 v93, v185
	v_mov_b32_e32 v94, v186
	v_mov_b32_e32 v95, v187
	v_mov_b32_e32 v96, v188
	v_mov_b32_e32 v97, v189
	v_mov_b32_e32 v98, v190
	v_mov_b32_e32 v99, v191
	v_mov_b32_e32 v100, v196
	v_mov_b32_e32 v101, v197
	v_mov_b32_e32 v102, v198
	v_mov_b32_e32 v103, v199
	v_pk_mul_f32 v[104:105], v[68:69], v[124:125] op_sel_hi:[0,1]
	v_pk_mul_f32 v[92:93], v[92:93], v[104:105]
	v_pk_add_f32 v[96:97], v[96:97], 1.0 op_sel_hi:[1,0]
	v_pk_mul_f32 v[94:95], v[94:95], v[106:107]
	v_pk_fma_f32 v[92:93], v[96:97], v[92:93], v[100:101]
	v_pk_add_f32 v[98:99], v[98:99], 1.0 op_sel_hi:[1,0]
	v_cvt_pk_fp8_f32 v108, v92, v93
	v_pk_fma_f32 v[94:95], v[98:99], v[94:95], v[102:103]
	s_nop 0
	v_cvt_pk_fp8_f32 v108, v94, v95 op_sel:[0,0,1]
	global_store_dword v[2:3], v108, off offset:768
	v_mov_b32_e32 v96, v200
	v_mov_b32_e32 v97, v201
	v_mov_b32_e32 v98, v202
	v_mov_b32_e32 v99, v203
	v_mov_b32_e32 v100, v204
	v_mov_b32_e32 v101, v205
	v_mov_b32_e32 v102, v206
	v_mov_b32_e32 v103, v207
	v_mov_b32_e32 v104, v208
	v_mov_b32_e32 v105, v209
	v_mov_b32_e32 v106, v210
	v_mov_b32_e32 v107, v211
	v_pk_mul_f32 v[108:109], v[68:69], v[126:127] op_sel_hi:[0,1]
	v_pk_mul_f32 v[96:97], v[96:97], v[108:109]
	v_pk_add_f32 v[100:101], v[100:101], 1.0 op_sel_hi:[1,0]
	v_pk_mul_f32 v[98:99], v[98:99], v[110:111]
	v_pk_fma_f32 v[96:97], v[100:101], v[96:97], v[104:105]
	v_pk_add_f32 v[102:103], v[102:103], 1.0 op_sel_hi:[1,0]
	v_cvt_pk_fp8_f32 v114, v96, v97
	v_pk_fma_f32 v[98:99], v[102:103], v[98:99], v[106:107]
	s_nop 0
	v_cvt_pk_fp8_f32 v114, v98, v99 op_sel:[0,0,1]
	global_store_dword v[2:3], v114, off offset:1024
	v_mov_b32_e32 v100, v212
	v_mov_b32_e32 v101, v213
	v_mov_b32_e32 v102, v214
	v_mov_b32_e32 v103, v215
	v_mov_b32_e32 v104, v216
	v_mov_b32_e32 v105, v217
	v_mov_b32_e32 v106, v218
	v_mov_b32_e32 v107, v219
	v_mov_b32_e32 v108, v220
	v_mov_b32_e32 v109, v221
	v_mov_b32_e32 v110, v222
	v_mov_b32_e32 v111, v223
	v_pk_mul_f32 v[66:67], v[100:101], v[66:67]
	v_pk_add_f32 v[100:101], v[104:105], 1.0 op_sel_hi:[1,0]
	v_pk_mul_f32 v[102:103], v[102:103], v[64:65]
	v_pk_fma_f32 v[64:65], v[100:101], v[66:67], v[108:109]
	v_pk_add_f32 v[104:105], v[106:107], 1.0 op_sel_hi:[1,0]
	v_cvt_pk_fp8_f32 v112, v64, v65
	v_pk_fma_f32 v[66:67], v[104:105], v[102:103], v[110:111]
	s_nop 0
	v_cvt_pk_fp8_f32 v112, v66, v67 op_sel:[0,0,1]
	global_store_dword v[2:3], v112, off offset:1280
	v_mov_b32_e32 v100, v224
	v_mov_b32_e32 v101, v225
	v_mov_b32_e32 v102, v226
	v_mov_b32_e32 v103, v227
	v_mov_b32_e32 v104, v228
	v_mov_b32_e32 v105, v229
	v_mov_b32_e32 v106, v230
	v_mov_b32_e32 v107, v231
	v_mov_b32_e32 v108, v232
	v_mov_b32_e32 v109, v233
	v_mov_b32_e32 v110, v234
	v_mov_b32_e32 v111, v235
	v_mov_b32_e32 v112, 0
	v_pk_mul_f32 v[62:63], v[100:101], v[62:63]
	v_pk_add_f32 v[100:101], v[104:105], 1.0 op_sel_hi:[1,0]
	v_pk_mul_f32 v[8:9], v[102:103], v[8:9]
	v_pk_fma_f32 v[100:101], v[100:101], v[62:63], v[108:109]
	v_pk_add_f32 v[62:63], v[106:107], 1.0 op_sel_hi:[1,0]
	v_cvt_pk_fp8_f32 v112, v100, v101
	v_pk_fma_f32 v[102:103], v[62:63], v[8:9], v[110:111]
	v_cndmask_b32_e64 v8, 0, 1, s[6:7]
	v_cmp_ne_u32_e32 vcc, 1, v8
	v_cvt_pk_fp8_f32 v112, v102, v103 op_sel:[0,0,1]
	v_pk_mul_f32 v[8:9], v[68:69], v[4:5] op_sel_hi:[0,1]
	v_mov_b32_e32 v62, 0
	s_mov_b64 s[6:7], 0
	global_store_dword v[2:3], v112, off offset:1536
	v_mov_b32_e32 v104, v238
	v_mov_b32_e32 v105, v239
	v_mov_b32_e32 v106, v240
	v_mov_b32_e32 v107, v241
	v_mov_b32_e32 v108, v242
	v_mov_b32_e32 v109, v243
	v_mov_b32_e32 v110, v244
	v_mov_b32_e32 v111, v245
	s_nop 0
	v_mov_b32_e32 v112, v246
	v_mov_b32_e32 v113, v247
	v_mov_b32_e32 v114, v248
	v_mov_b32_e32 v115, v249
	v_lshl_add_u32 v63, s16, 13, v73
	s_and_b64 vcc, exec, vcc
	ds_write_b128 v63, v[80:83]
	ds_write_b128 v63, v[84:87] offset:1024
	ds_write_b128 v63, v[88:91] offset:2048
	ds_write_b128 v63, v[92:95] offset:3072
	ds_write_b128 v63, v[96:99] offset:4096
	v_pk_mul_f32 v[4:5], v[104:105], v[6:7]
	v_pk_add_f32 v[6:7], v[108:109], 1.0 op_sel_hi:[1,0]
	v_pk_fma_f32 v[4:5], v[6:7], v[4:5], v[112:113]
	v_pk_mul_f32 v[6:7], v[106:107], v[8:9]
	v_cvt_pk_fp8_f32 v62, v4, v5
	v_pk_add_f32 v[8:9], v[110:111], 1.0 op_sel_hi:[1,0]
	s_nop 0
	v_pk_fma_f32 v[6:7], v[8:9], v[6:7], v[114:115]
	ds_write_b128 v63, v[64:67] offset:5120
	ds_write_b128 v63, v[100:103] offset:6144
	ds_write_b128 v63, v[4:7] offset:7168
	v_cvt_pk_fp8_f32 v62, v6, v7 op_sel:[0,0,1]
	global_store_dword v[2:3], v62, off offset:1792
	s_cbranch_vccz .LBB0_1409
	v_mov_b32_e32 v2, 0
	v_mov_b32_e32 v62, v69
	v_mov_b32_e32 v3, v2
	v_mov_b32_e32 v4, v2
	v_mov_b32_e32 v5, v2
	v_mov_b32_e32 v6, v2
	v_mov_b32_e32 v7, v2
	v_mov_b32_e32 v8, v2
	v_mov_b32_e32 v9, v2
	s_waitcnt lgkmcnt(0)
	s_barrier
